# v39 + indexer bitmask dword stores also at agent scope (write-through)
# baseline (speedup 1.0000x reference)
.LBB0_1975:
	s_lshl_b32 s80, s0, 23
	v_lshl_add_u64 v[2:3], v[106:107], 0, s[80:81]
	s_lshl_b32 s80, s34, 2
	s_or_b32 s29, s1, 7
	v_lshl_add_u64 v[2:3], v[2:3], 0, s[80:81]
	s_mov_b32 s65, s81
	v_readlane_b32 s91, v253, 27
	v_readlane_b32 s92, v253, 28
	s_mov_b32 s89, 0x2e8ba2e9
	s_movk_i32 s95, 0x100
	s_movk_i32 s90, 0xfea0
	s_movk_i32 s94, 0x2000
	v_lshl_add_u64 v[2:3], v[2:3], 0, s[64:65]
	v_cmp_ge_i32_e32 vcc, s29, v104
	v_readlane_b32 s93, v253, 29
	s_and_saveexec_b64 s[42:43], vcc
	s_cbranch_execz .LBB0_1977
	global_store_dword v[2:3], v0, off sc1
.LBB0_1977:
	s_or_b64 exec, exec, s[42:43]
	v_cmp_ge_i32_e32 vcc, s29, v105
	s_and_saveexec_b64 s[42:43], vcc
	s_cbranch_execz .LBB0_1979
	v_add_co_u32_e32 v2, vcc, 0x400000, v2
	s_nop 1
	v_addc_co_u32_e32 v3, vcc, 0, v3, vcc
	global_store_dword v[2:3], v4, off sc1
